# GEMM1 start staggered per XCD (2 us steps, workgroup id & 7) so the tile epilogue store bursts of different XCDs do not coincide
# baseline (speedup 1.0000x reference)
.LBB0_181:
	s_andn2_b64 vcc, exec, s[4:5]
	v_writelane_b32 v236, s43, 17
	s_cbranch_vccnz .LBB0_252
	s_and_b32 s98, s96, 7
	s_cmp_eq_u32 s98, 0
	s_cbranch_scc1 .Lg1_stag_done
.Lg1_stag_loop:
	s_sleep 66
	s_sub_u32 s98, s98, 1
	s_cmp_lg_u32 s98, 0
	s_cbranch_scc1 .Lg1_stag_loop
.Lg1_stag_done:
	v_readlane_b32 s4, v239, 51
	s_waitcnt vmcnt(0)
	v_mov_b32_e32 v8, v0
	v_readlane_b32 s5, v239, 52
	s_andn2_b64 vcc, exec, s[4:5]
	v_readfirstlane_b32 s6, v8
	s_cbranch_vccnz .LBB0_202
	v_lshlrev_b32_e32 v1, 4, v8
	v_add_u32_e32 v2, 0x2000, v1
	v_ashrrev_i32_e32 v4, 31, v2
	v_lshrrev_b32_e32 v4, 22, v4
	v_add_u32_e32 v4, v2, v4
	v_ashrrev_i32_e32 v9, 10, v4
	v_mul_i32_i24_e32 v4, 0x400, v9
	v_sub_u32_e32 v2, v2, v4
	v_lshrrev_b32_e32 v4, 4, v2
	v_bitop3_b32 v2, v4, v2, 32 bitop3:0x6c
	v_ashrrev_i32_e32 v4, 31, v2
	v_lshrrev_b32_e32 v4, 26, v4
	s_mul_i32 s14, s43, 0x1e00000
	v_add_u32_e32 v4, v2, v4
	v_lshlrev_b32_e32 v5, 3, v9
	s_lshl_b64 s[4:5], s[14:15], 1
	v_readlane_b32 s7, v237, 4
	v_ashrrev_i32_e32 v10, 6, v4
	v_and_b32_e32 v5, -16, v5
	s_add_u32 s48, s7, s4
	v_readlane_b32 s4, v237, 5
	v_add_u32_e32 v5, v10, v5
	s_addc_u32 s49, s4, s5
	v_and_b32_e32 v6, 3, v10
	s_mov_b32 s4, 0xfffe0
	v_lshrrev_b32_e32 v7, 2, v5
	v_lshlrev_b32_e32 v11, 1, v5
	v_and_b32_e32 v4, 0xc0, v4
	v_and_or_b32 v6, v5, s4, v6
	v_and_b32_e32 v7, 4, v7
	v_and_b32_e32 v11, 24, v11
	v_sub_u32_e32 v2, v2, v4
	v_or3_b32 v6, v6, v7, v11
	v_lshlrev_b32_e32 v7, 5, v9
	v_ashrrev_i16_sdwa v2, v208, sext(v2) dst_sel:DWORD dst_unused:UNUSED_PAD src0_sel:DWORD src1_sel:BYTE_0
	v_and_b32_e32 v7, 32, v7
	v_bfe_i32 v11, v2, 0, 16
	v_add_lshl_u32 v2, v7, v11, 1
	v_lshl_add_u32 v132, v6, 12, v2
	v_lshl_add_u32 v134, v5, 12, v2
	v_bfe_i32 v2, v8, 27, 1
	v_lshrrev_b32_e32 v2, 22, v2
	v_add_u32_e32 v2, v1, v2
	v_and_b32_e32 v2, 0xfffffc00, v2
	v_sub_u32_e32 v1, v1, v2
	v_lshrrev_b32_e32 v2, 4, v1
	v_ashrrev_i32_e32 v4, 31, v8
	v_bitop3_b32 v1, v2, v1, 32 bitop3:0x6c
	v_lshrrev_b32_e32 v4, 26, v4
	v_ashrrev_i32_e32 v2, 31, v1
	v_add_u32_e32 v4, v8, v4
	v_lshrrev_b32_e32 v2, 26, v2
	v_ashrrev_i32_e32 v13, 6, v4
	v_add_u32_e32 v2, v1, v2
	v_lshlrev_b32_e32 v4, 3, v13
	v_ashrrev_i32_e32 v12, 6, v2
	v_and_b32_e32 v4, -16, v4
	v_add_u32_e32 v4, v12, v4
	v_and_b32_e32 v5, 3, v12
	v_lshrrev_b32_e32 v6, 2, v4
	v_lshlrev_b32_e32 v7, 1, v4
	v_and_b32_e32 v2, 0xc0, v2
	s_ashr_i32 s8, s6, 6
	v_and_or_b32 v5, v4, s4, v5
	v_and_b32_e32 v6, 4, v6
	v_and_b32_e32 v7, 24, v7
	v_sub_u32_e32 v1, v1, v2
	s_ashr_i32 s7, s6, 8
	s_lshl_b32 s51, s8, 10
	v_or3_b32 v5, v5, v6, v7
	v_lshlrev_b32_e32 v6, 5, v13
	v_ashrrev_i16_sdwa v1, v208, sext(v1) dst_sel:DWORD dst_unused:UNUSED_PAD src0_sel:DWORD src1_sel:BYTE_0
	v_readlane_b32 s4, v238, 52
	v_and_b32_e32 v6, 32, v6
	v_bfe_i32 v14, v1, 0, 16
	v_readlane_b32 s5, v238, 53
	s_add_u32 s42, s48, s4
	v_add_lshl_u32 v1, v6, v14, 1
	s_addc_u32 s43, s49, s5
	s_add_i32 s60, s51, 0
	v_lshl_add_u32 v2, v5, 12, v1
	s_add_i32 m0, s60, 0x10000
	v_lshl_add_u32 v136, v4, 12, v1
	global_load_lds_dwordx4 v2, s[42:43]
	s_add_i32 m0, s60, 0x12000
	s_add_u32 s4, s42, 0x80000
	global_load_lds_dwordx4 v132, s[42:43]
	s_addc_u32 s5, s43, 0
	s_add_i32 m0, s60, 0x14000
	s_add_i32 s61, s60, 0x2000
	global_load_lds_dwordx4 v2, s[4:5]
	s_add_i32 m0, s60, 0x16000
	s_add_i32 s80, s60, 0x4000
	global_load_lds_dwordx4 v132, s[4:5]
	v_readlane_b32 s4, v237, 6
	s_mov_b32 m0, s60
	v_readlane_b32 s5, v237, 7
	s_add_i32 s81, s60, 0x6000
	v_mov_b32_e32 v133, v3
	s_cmp_eq_u32 s7, 1
	v_lshl_add_u64 v[4:5], s[42:43], 0, v[2:3]
	v_lshl_add_u64 v[6:7], s[42:43], 0, v[132:133]
	global_load_lds_dwordx4 v136, s[4:5]
	s_mov_b32 m0, s61
	s_nop 0
	global_load_lds_dwordx4 v134, s[4:5]
	v_readlane_b32 s4, v237, 8
	s_mov_b32 m0, s80
	v_readlane_b32 s5, v237, 9
	s_nop 4
	global_load_lds_dwordx4 v136, s[4:5]
	s_mov_b32 m0, s81
	s_nop 0
	global_load_lds_dwordx4 v134, s[4:5]
	s_cselect_b64 s[4:5], -1, 0
	s_cmp_lg_u32 s7, 1
	s_cbranch_scc1 .LBB0_185
	s_barrier
